# MFMA segments of both attention loops regenerated PV-first with first fragments prefetched before the segment barrier
# baseline (speedup 1.0000x reference)
; #define PK4(P, BASE, OUT) do { u32x4 w = {cvtpk(P[BASE + 0], P[BASE + 1]), cvtpk(P[BASE + 2], P[BASE + 3]), cvtpk(P[BASE + 4], P[BASE + 5]), cvtpk(P[BASE + 6], P[BASE + 7])}; \
;     OUT = *reinterpret_cast<bf16x8*>(&w); } while (0)
; __device__ __forceinline__ void smax_tile(f32x16& p0, f32x16& p1, float& mhat, float& l_reg, f32x16 (&o)[4], float* al_l, const bool first, int r32, int hi,
;                                           bf16x8& pa0, bf16x8& pa1, bf16x8& pa2, bf16x8& pa3) {
;     ...
; #pragma unroll
;     for (int r = 0; r < 16; ++r) p0[r] = __builtin_amdgcn_exp2f(p0[r]);
; #pragma unroll
;     for (int r = 0; r < 16; ++r) p1[r] = __builtin_amdgcn_exp2f(p1[r]);
;     float ps = p0[0];
; #pragma unroll
;     for (int r = 1; r < 16; ++r) ps += p0[r];
; #pragma unroll
;     for (int r = 0; r < 16; ++r) ps += p1[r];
;     { auto rr = __builtin_amdgcn_permlane32_swap(__float_as_uint(ps), __float_as_uint(ps), false, false); ps = __uint_as_float(rr[0]) + __uint_as_float(rr[1]); }
;     l_reg += ps;
;     ...
;     PK4(p0, 0, pa0); PK4(p0, 8, pa1); PK4(p1, 0, pa2); PK4(p1, 8, pa3);
.LBB0_605:
	v_exp_f32_e32 v96, v96
	v_exp_f32_e32 v97, v97
	v_exp_f32_e32 v98, v98
	v_exp_f32_e32 v99, v99
	v_exp_f32_e32 v100, v100
	v_exp_f32_e32 v101, v101
	v_add_f32_e32 v160, v96, v97
	v_exp_f32_e32 v102, v102
	v_add_f32_e32 v160, v98, v160
	v_exp_f32_e32 v103, v103
	v_add_f32_e32 v160, v99, v160
	v_exp_f32_e32 v104, v104
	v_add_f32_e32 v160, v100, v160
	v_exp_f32_e32 v105, v105
	v_add_f32_e32 v160, v101, v160
	v_exp_f32_e32 v106, v106
	v_add_f32_e32 v160, v102, v160
	v_exp_f32_e32 v107, v107
	v_add_f32_e32 v160, v103, v160
	v_exp_f32_e32 v108, v108
	v_add_f32_e32 v160, v104, v160
	v_exp_f32_e32 v109, v109
	v_add_f32_e32 v160, v105, v160
	v_exp_f32_e32 v110, v110
	v_add_f32_e32 v160, v106, v160
	v_exp_f32_e32 v111, v111
	v_add_f32_e32 v160, v107, v160
	v_exp_f32_e32 v80, v80
	v_add_f32_e32 v160, v108, v160
	v_exp_f32_e32 v81, v81
	v_add_f32_e32 v160, v109, v160
	v_exp_f32_e32 v82, v82
	v_add_f32_e32 v160, v110, v160
	v_exp_f32_e32 v83, v83
	v_add_f32_e32 v160, v111, v160
	v_exp_f32_e32 v84, v84
	v_add_f32_e32 v160, v80, v160
	v_exp_f32_e32 v85, v85
	v_add_f32_e32 v160, v81, v160
	v_exp_f32_e32 v86, v86
	v_add_f32_e32 v160, v82, v160
	v_exp_f32_e32 v87, v87
	v_add_f32_e32 v160, v83, v160
	v_exp_f32_e32 v88, v88
	v_add_f32_e32 v160, v84, v160
	v_exp_f32_e32 v89, v89
	v_add_f32_e32 v160, v85, v160
	v_exp_f32_e32 v90, v90
	v_add_f32_e32 v160, v86, v160
	v_exp_f32_e32 v91, v91
	v_add_f32_e32 v160, v87, v160
	v_exp_f32_e32 v92, v92
	v_add_f32_e32 v160, v88, v160
	v_exp_f32_e32 v93, v93
	v_add_f32_e32 v160, v89, v160
	v_exp_f32_e32 v94, v94
	v_add_f32_e32 v160, v90, v160
	v_exp_f32_e32 v95, v95
	v_add_f32_e32 v160, v91, v160
	v_add_f32_e32 v160, v92, v160
	v_add_f32_e32 v160, v93, v160
	v_add_f32_e32 v160, v94, v160
	v_add_f32_e32 v160, v95, v160
	v_mov_b32_e32 v161, v160
	s_nop 1
	v_permlane32_swap_b32_e32 v160, v161
	v_add_f32_e32 v160, v160, v161
	v_add_f32_e32 v204, v204, v160
	v_cvt_pk_bf16_f32 v172, v96, v97
	v_cvt_pk_bf16_f32 v173, v98, v99
	v_cvt_pk_bf16_f32 v174, v100, v101
	v_cvt_pk_bf16_f32 v175, v102, v103
	v_cvt_pk_bf16_f32 v168, v104, v105
	v_cvt_pk_bf16_f32 v169, v106, v107
	v_cvt_pk_bf16_f32 v170, v108, v109
	v_cvt_pk_bf16_f32 v171, v110, v111
	v_cvt_pk_bf16_f32 v164, v80, v81
	v_cvt_pk_bf16_f32 v165, v82, v83
	v_cvt_pk_bf16_f32 v166, v84, v85
	v_cvt_pk_bf16_f32 v167, v86, v87
	v_cvt_pk_bf16_f32 v160, v88, v89
	v_cvt_pk_bf16_f32 v161, v90, v91
	v_cvt_pk_bf16_f32 v162, v92, v93
	v_cvt_pk_bf16_f32 v163, v94, v95
	s_mul_i32 s47, s26, 0x6000
	s_addk_i32 s93, 0xc000
	s_cmp_lg_u32 s26, 0
	s_cselect_b32 s46, s93, 0x8000
	v_add_u32_e32 v227, s46, v202
	v_add_u32_e32 v207, s47, v185
	v_add_u32_e32 v224, s47, v187
	v_add_u32_e32 v225, s47, v205
	v_add_u32_e32 v226, s47, v206
	s_waitcnt lgkmcnt(0)
	ds_read_b64_tr_b16 v[208:209], v227 offset:0
	ds_read_b64_tr_b16 v[210:211], v227 offset:2048
	ds_read_b64_tr_b16 v[212:213], v227 offset:512
	ds_read_b64_tr_b16 v[214:215], v227 offset:2560
	ds_read_b64_tr_b16 v[216:217], v227 offset:1024
	ds_read_b64_tr_b16 v[218:219], v227 offset:3072
	ds_read_b64_tr_b16 v[220:221], v227 offset:1536
	ds_read_b64_tr_b16 v[222:223], v227 offset:3584
	s_barrier
; template <int DQK, bool HASQK, bool HASPV, int J>
; __device__ __forceinline__ void slot_read(bf16x8 (&kf)[DQK / 16][2], s16x4 (&vf)[4][8], const int (&ka_)[4], int vb_) {
;     constexpr int NQS = HASQK ? 2 * (DQK / 16) : 0, NS = NQS + (HASPV ? 16 : 0);
;     if constexpr (J < NQS) { constexpr int d0 = J >> 1, h = J & 1; dsr128<(d0 >> 2) * 128 + h * 32 * DQK * 2>(kf[d0][h], ka_[d0 & 3]); }
;     else if constexpr (J < NS) { constexpr int q = J - NQS, g = q >> 2, d = q & 3; dstr64<v_rd_off(d, g, 0)>(vf[g][2 * d], vb_); dstr64<v_rd_off(d, g, 1)>(vf[g][2 * d + 1], vb_); }
; }
; template <int DQK, bool HASQK, bool HASPV, int J> ...
;     constexpr int NQS = HASQK ? 2 * (DQK / 16) : 0, NS = NQS + (HASPV ? 16 : 0);
;     if constexpr (J < NS) {
;         constexpr int rd1 = (J + 1 < NS) ? ((J + 1 < NQS) ? 1 : 2) : 0, rd2 = (J + 2 < NS) ? ((J + 2 < NQS) ? 1 : 2) : 0, rd3 = (J + 3 < NS) ? ((J + 3 < NQS) ? 1 : 2) : 0, NW = rd1 + rd2 + rd3;
;     ...
;         if constexpr (J < NQS) { constexpr int d0 = J >> 1, h = J & 1;
;             LWN1(kf[d0][h]); SBAR();
;             if constexpr (h == 0) p0 = __builtin_amdgcn_mfma_f32_32x32x16_bf16(kf[d0][0], qr[d0], (d0 == 0) ? negm : p0, 0, 0, 0);
;             else p1 = __builtin_amdgcn_mfma_f32_32x32x16_bf16(kf[d0][1], qr[d0], (d0 == 0) ? negm : p1, 0, 0, 0);
;         } else { constexpr int q = J - NQS, g = q >> 2, d = q & 3;
;             LWN2(vf[g][2 * d], vf[g][2 * d + 1]); SBAR();
;             o[d] = __builtin_amdgcn_mfma_f32_32x32x16_bf16(pa[g], (bf16x8){vf[g][2 * d][0], vf[g][2 * d][1], vf[g][2 * d][2], vf[g][2 * d][3], vf[g][2 * d + 1][0], vf[g][2 * d + 1][1], vf[g][2 * d + 1][2], vf[g][2 * d + 1][3]}, o[d], 0, 0, 0);
;         }
;     ...
;         SBAR();
;         slot_read<DQK, HASQK, HASPV, J + 4>(kf, vf, ka_, vb_);
;         SBAR();
;         slot_run<DQK, HASQK, HASPV, J + 1>(kf, vf, ka_, vb_, qr, p0, p1, negm, o, pa);
;     }
; }
;     ...
;     for (int i = 0; i < NT - 1; ++i) {
;         SEG_S(i);
;         { const int cp = (ci == 0) ? 2 : ci - 1, cn = (ci == 2) ? 0 : ci + 1;
;           if (DMA_M) { if (i + 3 < NT) DMA_K(i + 3, cp); if (i + 2 < NT) DMA_V(i + 2, cn); }
;           SEG_M(true, true, ci, cp);
;           if (DMA_M && i + 3 < NT) asm volatile("s_waitcnt vmcnt(%0)" :: "n"(NKW + 2) : "memory");
;           else asm volatile("s_waitcnt vmcnt(0)" ::: "memory");
;           BAR_ALL(); }
	s_waitcnt lgkmcnt(6)
	v_mfma_f32_32x32x16_bf16 v[64:79], v[172:175], v[208:211], v[64:79]
	ds_read_b64_tr_b16 v[208:209], v227 offset:4096
	ds_read_b64_tr_b16 v[210:211], v227 offset:6144
	s_waitcnt lgkmcnt(6)
	v_mfma_f32_32x32x16_bf16 v[48:63], v[172:175], v[212:215], v[48:63]
	ds_read_b64_tr_b16 v[212:213], v227 offset:4608
	ds_read_b64_tr_b16 v[214:215], v227 offset:6656
	s_waitcnt lgkmcnt(6)
	v_mfma_f32_32x32x16_bf16 v[32:47], v[172:175], v[216:219], v[32:47]
	ds_read_b64_tr_b16 v[216:217], v227 offset:5120
	ds_read_b64_tr_b16 v[218:219], v227 offset:7168
	s_waitcnt lgkmcnt(6)
	v_mfma_f32_32x32x16_bf16 v[16:31], v[172:175], v[220:223], v[16:31]
	ds_read_b64_tr_b16 v[220:221], v227 offset:5632
	ds_read_b64_tr_b16 v[222:223], v227 offset:7680
	s_waitcnt lgkmcnt(6)
	v_mfma_f32_32x32x16_bf16 v[64:79], v[168:171], v[208:211], v[64:79]
	ds_read_b64_tr_b16 v[208:209], v227 offset:8192
	ds_read_b64_tr_b16 v[210:211], v227 offset:10240
	s_waitcnt lgkmcnt(6)
	v_mfma_f32_32x32x16_bf16 v[48:63], v[168:171], v[212:215], v[48:63]
	ds_read_b64_tr_b16 v[212:213], v227 offset:8704
	ds_read_b64_tr_b16 v[214:215], v227 offset:10752
	s_waitcnt lgkmcnt(6)
	v_mfma_f32_32x32x16_bf16 v[32:47], v[168:171], v[216:219], v[32:47]
	ds_read_b64_tr_b16 v[216:217], v227 offset:9216
	ds_read_b64_tr_b16 v[218:219], v227 offset:11264
	s_waitcnt lgkmcnt(6)
	v_mfma_f32_32x32x16_bf16 v[16:31], v[168:171], v[220:223], v[16:31]
	ds_read_b64_tr_b16 v[220:221], v227 offset:9728
	ds_read_b64_tr_b16 v[222:223], v227 offset:11776
	s_waitcnt lgkmcnt(6)
	v_mfma_f32_32x32x16_bf16 v[64:79], v[164:167], v[208:211], v[64:79]
	ds_read_b64_tr_b16 v[208:209], v227 offset:12288
	ds_read_b64_tr_b16 v[210:211], v227 offset:14336
	s_waitcnt lgkmcnt(6)
	v_mfma_f32_32x32x16_bf16 v[48:63], v[164:167], v[212:215], v[48:63]
	ds_read_b64_tr_b16 v[212:213], v227 offset:12800
	ds_read_b64_tr_b16 v[214:215], v227 offset:14848
	s_waitcnt lgkmcnt(6)
	v_mfma_f32_32x32x16_bf16 v[32:47], v[164:167], v[216:219], v[32:47]
	ds_read_b64_tr_b16 v[216:217], v227 offset:13312
	ds_read_b64_tr_b16 v[218:219], v227 offset:15360
	s_waitcnt lgkmcnt(6)
	v_mfma_f32_32x32x16_bf16 v[16:31], v[164:167], v[220:223], v[16:31]
	ds_read_b64_tr_b16 v[220:221], v227 offset:13824
	ds_read_b64_tr_b16 v[222:223], v227 offset:15872
	v_xor_b32_e32 v80, 0x80000000, v203
	v_mov_b32_e32 v81, v80
	v_mov_b32_e32 v82, v80
	v_mov_b32_e32 v83, v80
	v_mov_b32_e32 v84, v80
	v_mov_b32_e32 v85, v80
	v_mov_b32_e32 v86, v80
	v_mov_b32_e32 v87, v80
	v_mov_b32_e32 v88, v80
	v_mov_b32_e32 v89, v80
	v_mov_b32_e32 v90, v80
	v_mov_b32_e32 v91, v80
	v_mov_b32_e32 v92, v80
	v_mov_b32_e32 v93, v80
	v_mov_b32_e32 v94, v80
	v_mov_b32_e32 v95, v80
	s_waitcnt lgkmcnt(6)
	v_mfma_f32_32x32x16_bf16 v[64:79], v[160:163], v[208:211], v[64:79]
	ds_read_b128 v[208:211], v207 offset:0
	s_waitcnt lgkmcnt(5)
	v_mfma_f32_32x32x16_bf16 v[48:63], v[160:163], v[212:215], v[48:63]
	ds_read_b128 v[212:215], v207 offset:12288
	s_waitcnt lgkmcnt(4)
	v_mfma_f32_32x32x16_bf16 v[32:47], v[160:163], v[216:219], v[32:47]
	ds_read_b128 v[216:219], v224 offset:0
	s_waitcnt lgkmcnt(3)
	v_mfma_f32_32x32x16_bf16 v[16:31], v[160:163], v[220:223], v[16:31]
	ds_read_b128 v[220:223], v224 offset:12288
	s_waitcnt lgkmcnt(3)
	v_mfma_f32_32x32x16_bf16 v[96:111], v[208:211], v[112:115], v[80:95]
	ds_read_b128 v[208:211], v225 offset:0
	s_waitcnt lgkmcnt(3)
	v_mfma_f32_32x32x16_bf16 v[80:95], v[212:215], v[112:115], v[80:95]
	ds_read_b128 v[212:215], v225 offset:12288
	s_waitcnt lgkmcnt(3)
	v_mfma_f32_32x32x16_bf16 v[96:111], v[216:219], v[116:119], v[96:111]
	ds_read_b128 v[216:219], v226 offset:0
	s_waitcnt lgkmcnt(3)
	v_mfma_f32_32x32x16_bf16 v[80:95], v[220:223], v[116:119], v[80:95]
	ds_read_b128 v[220:223], v226 offset:12288
	s_waitcnt lgkmcnt(3)
	v_mfma_f32_32x32x16_bf16 v[96:111], v[208:211], v[120:123], v[96:111]
	ds_read_b128 v[208:211], v207 offset:128
	s_waitcnt lgkmcnt(3)
	v_mfma_f32_32x32x16_bf16 v[80:95], v[212:215], v[120:123], v[80:95]
	ds_read_b128 v[212:215], v207 offset:12416
	s_waitcnt lgkmcnt(3)
	v_mfma_f32_32x32x16_bf16 v[96:111], v[216:219], v[124:127], v[96:111]
	ds_read_b128 v[216:219], v224 offset:128
	s_waitcnt lgkmcnt(3)
	v_mfma_f32_32x32x16_bf16 v[80:95], v[220:223], v[124:127], v[80:95]
	ds_read_b128 v[220:223], v224 offset:12416
	s_waitcnt lgkmcnt(3)
	v_mfma_f32_32x32x16_bf16 v[96:111], v[208:211], v[128:131], v[96:111]
	ds_read_b128 v[208:211], v225 offset:128
	s_waitcnt lgkmcnt(3)
	v_mfma_f32_32x32x16_bf16 v[80:95], v[212:215], v[128:131], v[80:95]
	ds_read_b128 v[212:215], v225 offset:12416
	s_waitcnt lgkmcnt(3)
	v_mfma_f32_32x32x16_bf16 v[96:111], v[216:219], v[132:135], v[96:111]
	ds_read_b128 v[216:219], v226 offset:128
	s_waitcnt lgkmcnt(3)
	v_mfma_f32_32x32x16_bf16 v[80:95], v[220:223], v[132:135], v[80:95]
	ds_read_b128 v[220:223], v226 offset:12416
	s_waitcnt lgkmcnt(3)
	v_mfma_f32_32x32x16_bf16 v[96:111], v[208:211], v[136:139], v[96:111]
	ds_read_b128 v[208:211], v207 offset:256
	s_waitcnt lgkmcnt(3)
	v_mfma_f32_32x32x16_bf16 v[80:95], v[212:215], v[136:139], v[80:95]
	ds_read_b128 v[212:215], v207 offset:12544
	s_waitcnt lgkmcnt(3)
	v_mfma_f32_32x32x16_bf16 v[96:111], v[216:219], v[140:143], v[96:111]
	ds_read_b128 v[216:219], v224 offset:256
	s_waitcnt lgkmcnt(3)
	v_mfma_f32_32x32x16_bf16 v[80:95], v[220:223], v[140:143], v[80:95]
	ds_read_b128 v[220:223], v224 offset:12544
	s_waitcnt lgkmcnt(3)
	v_mfma_f32_32x32x16_bf16 v[96:111], v[208:211], v[144:147], v[96:111]
	ds_read_b128 v[208:211], v225 offset:256
	s_waitcnt lgkmcnt(3)
	v_mfma_f32_32x32x16_bf16 v[80:95], v[212:215], v[144:147], v[80:95]
	ds_read_b128 v[212:215], v225 offset:12544
	s_waitcnt lgkmcnt(3)
	v_mfma_f32_32x32x16_bf16 v[96:111], v[216:219], v[148:151], v[96:111]
	ds_read_b128 v[216:219], v226 offset:256
	s_waitcnt lgkmcnt(3)
	v_mfma_f32_32x32x16_bf16 v[80:95], v[220:223], v[148:151], v[80:95]
	ds_read_b128 v[220:223], v226 offset:12544
	s_waitcnt lgkmcnt(3)
	v_mfma_f32_32x32x16_bf16 v[96:111], v[208:211], v[152:155], v[96:111]
	s_waitcnt lgkmcnt(2)
	v_mfma_f32_32x32x16_bf16 v[80:95], v[212:215], v[152:155], v[80:95]
	s_waitcnt lgkmcnt(1)
	v_mfma_f32_32x32x16_bf16 v[96:111], v[216:219], v[156:159], v[96:111]
	s_waitcnt lgkmcnt(0)
	v_mfma_f32_32x32x16_bf16 v[80:95], v[220:223], v[156:159], v[80:95]
	s_waitcnt vmcnt(0)
	s_waitcnt lgkmcnt(0)
	s_barrier
	s_add_u32 s44, s44, 0x18000
	s_addc_u32 s45, s45, 0
	v_lshl_add_u64 v[194:195], v[194:195], 0, s[28:29]
	s_cmp_eq_u32 s44, 0xbe8000
	v_lshl_add_u64 v[196:197], v[196:197], 0, s[28:29]
	s_cbranch_scc1 .LBB0_616

; #define PK4(P, BASE, OUT) do { u32x4 w = {cvtpk(P[BASE + 0], P[BASE + 1]), cvtpk(P[BASE + 2], P[BASE + 3]), cvtpk(P[BASE + 4], P[BASE + 5]), cvtpk(P[BASE + 6], P[BASE + 7])}; \
;     OUT = *reinterpret_cast<bf16x8*>(&w); } while (0)
; __device__ __forceinline__ void smax_tile(f32x16& p0, f32x16& p1, float& mhat, float& l_reg, f32x16 (&o)[4], float* al_l, const bool first, int r32, int hi,
;                                           bf16x8& pa0, bf16x8& pa1, bf16x8& pa2, bf16x8& pa3) {
;     ...
; #pragma unroll
;     for (int r = 0; r < 16; ++r) p0[r] = __builtin_amdgcn_exp2f(p0[r]);
; #pragma unroll
;     for (int r = 0; r < 16; ++r) p1[r] = __builtin_amdgcn_exp2f(p1[r]);
;     float ps = p0[0];
; #pragma unroll
;     for (int r = 1; r < 16; ++r) ps += p0[r];
; #pragma unroll
;     for (int r = 0; r < 16; ++r) ps += p1[r];
;     { auto rr = __builtin_amdgcn_permlane32_swap(__float_as_uint(ps), __float_as_uint(ps), false, false); ps = __uint_as_float(rr[0]) + __uint_as_float(rr[1]); }
;     l_reg += ps;
;     ...
;     PK4(p0, 0, pa0); PK4(p0, 8, pa1); PK4(p1, 0, pa2); PK4(p1, 8, pa3);
.LBB0_651:
	v_exp_f32_e32 v96, v96
	v_exp_f32_e32 v97, v97
	v_exp_f32_e32 v98, v98
	v_exp_f32_e32 v99, v99
	v_exp_f32_e32 v100, v100
	v_exp_f32_e32 v101, v101
	v_add_f32_e32 v128, v96, v97
	v_exp_f32_e32 v102, v102
	v_add_f32_e32 v128, v98, v128
	v_exp_f32_e32 v103, v103
	v_add_f32_e32 v128, v99, v128
	v_exp_f32_e32 v104, v104
	v_add_f32_e32 v128, v100, v128
	v_exp_f32_e32 v105, v105
	v_add_f32_e32 v128, v101, v128
	v_exp_f32_e32 v106, v106
	v_add_f32_e32 v128, v102, v128
	v_exp_f32_e32 v107, v107
	v_add_f32_e32 v128, v103, v128
	v_exp_f32_e32 v108, v108
	v_add_f32_e32 v128, v104, v128
	v_exp_f32_e32 v109, v109
	v_add_f32_e32 v128, v105, v128
	v_exp_f32_e32 v110, v110
	v_add_f32_e32 v128, v106, v128
	v_exp_f32_e32 v111, v111
	v_add_f32_e32 v128, v107, v128
	v_exp_f32_e32 v80, v80
	v_add_f32_e32 v128, v108, v128
	v_exp_f32_e32 v81, v81
	v_add_f32_e32 v128, v109, v128
	v_exp_f32_e32 v82, v82
	v_add_f32_e32 v128, v110, v128
	v_exp_f32_e32 v83, v83
	v_add_f32_e32 v128, v111, v128
	v_exp_f32_e32 v84, v84
	v_add_f32_e32 v128, v80, v128
	v_exp_f32_e32 v85, v85
	v_add_f32_e32 v128, v81, v128
	v_exp_f32_e32 v86, v86
	v_add_f32_e32 v128, v82, v128
	v_exp_f32_e32 v87, v87
	v_add_f32_e32 v128, v83, v128
	v_exp_f32_e32 v88, v88
	v_add_f32_e32 v128, v84, v128
	v_exp_f32_e32 v89, v89
	v_add_f32_e32 v128, v85, v128
	v_exp_f32_e32 v90, v90
	v_add_f32_e32 v128, v86, v128
	v_exp_f32_e32 v91, v91
	v_add_f32_e32 v128, v87, v128
	v_exp_f32_e32 v92, v92
	v_add_f32_e32 v128, v88, v128
	v_exp_f32_e32 v93, v93
	v_add_f32_e32 v128, v89, v128
	v_exp_f32_e32 v94, v94
	v_add_f32_e32 v128, v90, v128
	v_exp_f32_e32 v95, v95
	v_add_f32_e32 v128, v91, v128
	v_add_f32_e32 v128, v92, v128
	v_add_f32_e32 v128, v93, v128
	v_add_f32_e32 v128, v94, v128
	v_add_f32_e32 v128, v95, v128
	v_mov_b32_e32 v129, v128
	s_nop 1
	v_permlane32_swap_b32_e32 v128, v129
	v_add_f32_e32 v128, v128, v129
	s_addk_i32 s87, 0xc000
	v_add_f32_e32 v159, v159, v128
	v_cvt_pk_bf16_f32 v162, v96, v97
	v_cvt_pk_bf16_f32 v163, v98, v99
	v_cvt_pk_bf16_f32 v164, v100, v101
	v_cvt_pk_bf16_f32 v165, v102, v103
	v_cvt_pk_bf16_f32 v166, v104, v105
	v_cvt_pk_bf16_f32 v167, v106, v107
	v_cvt_pk_bf16_f32 v168, v108, v109
	v_cvt_pk_bf16_f32 v169, v110, v111
	v_cvt_pk_bf16_f32 v132, v80, v81
	v_cvt_pk_bf16_f32 v133, v82, v83
	v_cvt_pk_bf16_f32 v134, v84, v85
	v_cvt_pk_bf16_f32 v135, v86, v87
	v_cvt_pk_bf16_f32 v128, v88, v89
	v_cvt_pk_bf16_f32 v129, v90, v91
	v_cvt_pk_bf16_f32 v130, v92, v93
	v_cvt_pk_bf16_f32 v131, v94, v95
	s_cmp_lg_u32 s86, 0
	s_cselect_b32 s46, s87, 0x8000
	s_lshl_b32 s47, s86, 13
	v_add_u32_e32 v188, s46, v157
	v_add_u32_e32 v232, s47, v141
	v_add_u32_e32 v233, s47, v143
	v_add_u32_e32 v186, s47, v160
	v_add_u32_e32 v187, s47, v161
	s_waitcnt lgkmcnt(0)
	ds_read_b64_tr_b16 v[170:171], v188 offset:0
	ds_read_b64_tr_b16 v[172:173], v188 offset:2048
	ds_read_b64_tr_b16 v[174:175], v188 offset:512
	ds_read_b64_tr_b16 v[176:177], v188 offset:2560
	ds_read_b64_tr_b16 v[178:179], v188 offset:1024
	ds_read_b64_tr_b16 v[180:181], v188 offset:3072
	ds_read_b64_tr_b16 v[182:183], v188 offset:1536
	ds_read_b64_tr_b16 v[184:185], v188 offset:3584
	s_barrier
; template <int DQK, bool HASQK, bool HASPV, int J>
; __device__ __forceinline__ void slot_read(bf16x8 (&kf)[DQK / 16][2], s16x4 (&vf)[4][8], const int (&ka_)[4], int vb_) {
;     constexpr int NQS = HASQK ? 2 * (DQK / 16) : 0, NS = NQS + (HASPV ? 16 : 0);
;     if constexpr (J < NQS) { constexpr int d0 = J >> 1, h = J & 1; dsr128<(d0 >> 2) * 128 + h * 32 * DQK * 2>(kf[d0][h], ka_[d0 & 3]); }
;     else if constexpr (J < NS) { constexpr int q = J - NQS, g = q >> 2, d = q & 3; dstr64<v_rd_off(d, g, 0)>(vf[g][2 * d], vb_); dstr64<v_rd_off(d, g, 1)>(vf[g][2 * d + 1], vb_); }
; }
; template <int DQK, bool HASQK, bool HASPV, int J> ...
;     constexpr int NQS = HASQK ? 2 * (DQK / 16) : 0, NS = NQS + (HASPV ? 16 : 0);
;     if constexpr (J < NS) {
;         constexpr int rd1 = (J + 1 < NS) ? ((J + 1 < NQS) ? 1 : 2) : 0, rd2 = (J + 2 < NS) ? ((J + 2 < NQS) ? 1 : 2) : 0, rd3 = (J + 3 < NS) ? ((J + 3 < NQS) ? 1 : 2) : 0, NW = rd1 + rd2 + rd3;
;     ...
;         if constexpr (J < NQS) { constexpr int d0 = J >> 1, h = J & 1;
;             LWN1(kf[d0][h]); SBAR();
;             if constexpr (h == 0) p0 = __builtin_amdgcn_mfma_f32_32x32x16_bf16(kf[d0][0], qr[d0], (d0 == 0) ? negm : p0, 0, 0, 0);
;             else p1 = __builtin_amdgcn_mfma_f32_32x32x16_bf16(kf[d0][1], qr[d0], (d0 == 0) ? negm : p1, 0, 0, 0);
;         } else { constexpr int q = J - NQS, g = q >> 2, d = q & 3;
;             LWN2(vf[g][2 * d], vf[g][2 * d + 1]); SBAR();
;             o[d] = __builtin_amdgcn_mfma_f32_32x32x16_bf16(pa[g], (bf16x8){vf[g][2 * d][0], vf[g][2 * d][1], vf[g][2 * d][2], vf[g][2 * d][3], vf[g][2 * d + 1][0], vf[g][2 * d + 1][1], vf[g][2 * d + 1][2], vf[g][2 * d + 1][3]}, o[d], 0, 0, 0);
;         }
;     ...
;         SBAR();
;         slot_read<DQK, HASQK, HASPV, J + 4>(kf, vf, ka_, vb_);
;         SBAR();
;         slot_run<DQK, HASQK, HASPV, J + 1>(kf, vf, ka_, vb_, qr, p0, p1, negm, o, pa);
;     }
; }
;     ...
;     for (int i = 0; i < NT - 1; ++i) {
;         SEG_S(i);
;         { const int cp = (ci == 0) ? 2 : ci - 1, cn = (ci == 2) ? 0 : ci + 1;
;           if (DMA_M) { if (i + 3 < NT) DMA_K(i + 3, cp); if (i + 2 < NT) DMA_V(i + 2, cn); }
;           SEG_M(true, true, ci, cp);
;           if (DMA_M && i + 3 < NT) asm volatile("s_waitcnt vmcnt(%0)" :: "n"(NKW + 2) : "memory");
;           else asm volatile("s_waitcnt vmcnt(0)" ::: "memory");
;           BAR_ALL(); }
	s_waitcnt lgkmcnt(6)
	v_mfma_f32_32x32x16_bf16 v[64:79], v[162:165], v[170:173], v[64:79]
	ds_read_b64_tr_b16 v[170:171], v188 offset:4096
	ds_read_b64_tr_b16 v[172:173], v188 offset:6144
	s_waitcnt lgkmcnt(6)
	v_mfma_f32_32x32x16_bf16 v[48:63], v[162:165], v[174:177], v[48:63]
	ds_read_b64_tr_b16 v[174:175], v188 offset:4608
	ds_read_b64_tr_b16 v[176:177], v188 offset:6656
	s_waitcnt lgkmcnt(6)
	v_mfma_f32_32x32x16_bf16 v[32:47], v[162:165], v[178:181], v[32:47]
	ds_read_b64_tr_b16 v[178:179], v188 offset:5120
	ds_read_b64_tr_b16 v[180:181], v188 offset:7168
	s_waitcnt lgkmcnt(6)
	v_mfma_f32_32x32x16_bf16 v[16:31], v[162:165], v[182:185], v[16:31]
	ds_read_b64_tr_b16 v[182:183], v188 offset:5632
	ds_read_b64_tr_b16 v[184:185], v188 offset:7680
	s_waitcnt lgkmcnt(6)
	v_mfma_f32_32x32x16_bf16 v[64:79], v[166:169], v[170:173], v[64:79]
	ds_read_b64_tr_b16 v[170:171], v188 offset:8192
	ds_read_b64_tr_b16 v[172:173], v188 offset:10240
	s_waitcnt lgkmcnt(6)
	v_mfma_f32_32x32x16_bf16 v[48:63], v[166:169], v[174:177], v[48:63]
	ds_read_b64_tr_b16 v[174:175], v188 offset:8704
	ds_read_b64_tr_b16 v[176:177], v188 offset:10752
	s_waitcnt lgkmcnt(6)
	v_mfma_f32_32x32x16_bf16 v[32:47], v[166:169], v[178:181], v[32:47]
	ds_read_b64_tr_b16 v[178:179], v188 offset:9216
	ds_read_b64_tr_b16 v[180:181], v188 offset:11264
	s_waitcnt lgkmcnt(6)
	v_mfma_f32_32x32x16_bf16 v[16:31], v[166:169], v[182:185], v[16:31]
	ds_read_b64_tr_b16 v[182:183], v188 offset:9728
	ds_read_b64_tr_b16 v[184:185], v188 offset:11776
	s_waitcnt lgkmcnt(6)
	v_mfma_f32_32x32x16_bf16 v[64:79], v[132:135], v[170:173], v[64:79]
	ds_read_b64_tr_b16 v[170:171], v188 offset:12288
	ds_read_b64_tr_b16 v[172:173], v188 offset:14336
	s_waitcnt lgkmcnt(6)
	v_mfma_f32_32x32x16_bf16 v[48:63], v[132:135], v[174:177], v[48:63]
	ds_read_b64_tr_b16 v[174:175], v188 offset:12800
	ds_read_b64_tr_b16 v[176:177], v188 offset:14848
	s_waitcnt lgkmcnt(6)
	v_mfma_f32_32x32x16_bf16 v[32:47], v[132:135], v[178:181], v[32:47]
	ds_read_b64_tr_b16 v[178:179], v188 offset:13312
	ds_read_b64_tr_b16 v[180:181], v188 offset:15360
	s_waitcnt lgkmcnt(6)
	v_mfma_f32_32x32x16_bf16 v[16:31], v[132:135], v[182:185], v[16:31]
	ds_read_b64_tr_b16 v[182:183], v188 offset:13824
	ds_read_b64_tr_b16 v[184:185], v188 offset:15872
	v_xor_b32_e32 v80, 0x80000000, v158
	v_mov_b32_e32 v81, v80
	v_mov_b32_e32 v82, v80
	v_mov_b32_e32 v83, v80
	v_mov_b32_e32 v84, v80
	v_mov_b32_e32 v85, v80
	v_mov_b32_e32 v86, v80
	v_mov_b32_e32 v87, v80
	v_mov_b32_e32 v88, v80
	v_mov_b32_e32 v89, v80
	v_mov_b32_e32 v90, v80
	v_mov_b32_e32 v91, v80
	v_mov_b32_e32 v92, v80
	v_mov_b32_e32 v93, v80
	v_mov_b32_e32 v94, v80
	v_mov_b32_e32 v95, v80
	s_waitcnt lgkmcnt(6)
	v_mfma_f32_32x32x16_bf16 v[64:79], v[128:131], v[170:173], v[64:79]
	ds_read_b128 v[170:173], v232 offset:0
	s_waitcnt lgkmcnt(5)
	v_mfma_f32_32x32x16_bf16 v[48:63], v[128:131], v[174:177], v[48:63]
	ds_read_b128 v[174:177], v232 offset:4096
	s_waitcnt lgkmcnt(4)
	v_mfma_f32_32x32x16_bf16 v[32:47], v[128:131], v[178:181], v[32:47]
	ds_read_b128 v[178:181], v233 offset:0
	s_waitcnt lgkmcnt(3)
	v_mfma_f32_32x32x16_bf16 v[16:31], v[128:131], v[182:185], v[16:31]
	ds_read_b128 v[182:185], v233 offset:4096
	s_waitcnt lgkmcnt(3)
	v_mfma_f32_32x32x16_bf16 v[96:111], v[170:173], v[112:115], v[80:95]
	ds_read_b128 v[170:173], v186 offset:0
	s_waitcnt lgkmcnt(3)
	v_mfma_f32_32x32x16_bf16 v[80:95], v[174:177], v[112:115], v[80:95]
	ds_read_b128 v[174:177], v186 offset:4096
	s_waitcnt lgkmcnt(3)
	v_mfma_f32_32x32x16_bf16 v[96:111], v[178:181], v[116:119], v[96:111]
	ds_read_b128 v[178:181], v187 offset:0
	s_waitcnt lgkmcnt(3)
	v_mfma_f32_32x32x16_bf16 v[80:95], v[182:185], v[116:119], v[80:95]
	ds_read_b128 v[182:185], v187 offset:4096
	s_waitcnt lgkmcnt(3)
	v_mfma_f32_32x32x16_bf16 v[96:111], v[170:173], v[120:123], v[96:111]
	s_waitcnt lgkmcnt(2)
	v_mfma_f32_32x32x16_bf16 v[80:95], v[174:177], v[120:123], v[80:95]
	s_waitcnt lgkmcnt(1)
	v_mfma_f32_32x32x16_bf16 v[96:111], v[178:181], v[124:127], v[96:111]
	s_waitcnt lgkmcnt(0)
	v_mfma_f32_32x32x16_bf16 v[80:95], v[182:185], v[124:127], v[80:95]
	s_waitcnt vmcnt(0)
	s_add_u32 s44, s44, 0x10000
	s_waitcnt lgkmcnt(0)
	s_barrier
	s_addc_u32 s45, s45, 0
	s_cmp_eq_u32 s44, 0x7f0000
	s_cbranch_scc1 .LBB0_662
